# stack2: previous stack + prologue w_in transpose load hoist + mLSTM-out item-top small loads issued with the K/Q loads before the barrier
# baseline (speedup 1.0000x reference)
; __device__ __forceinline__ void ph_mlstm_out(const Frame& F) {
;     ...
;     for (int item = F.bid; item < 1024; item += F.nwg) {
;         const int b = item / 512, h = (item / 64) % 8, c = item % 64;
;         const int t0 = b * S + c * 128;
;         bf16x8 cf[2][4];
; #pragma unroll
;         for (int vt = 0; vt < 2; ++vt)
; #pragma unroll
;             for (int st = 0; st < 4; ++st) cf[vt][st] = *(const bf16x8*)(CPREV + ((size_t)item * 256 + 16 * (2 * wave + vt) + l15) * 128 + 8 * g + 32 * st);
;         __syncthreads();
;         if (tid < 128) { const float bv = BCUM[(size_t)item * 128 + tid], iv = IPRE[(size_t)item * 128 + tid]; bc[tid] = bv; ipr[tid] = iv; dd[tid] = iv - bv; np[tid] = NPREV[(size_t)item * 128 + tid]; }
;         const float mprev = MPREV[item];
.LBB0_592:
	s_ashr_i32 s57, s56, 31
	s_lshl_b64 s[54:55], s[56:57], 8
	v_mov_b32_e32 v67, s55
	v_or_b32_e32 v66, s54, v172
	v_lshl_add_u64 v[68:69], v[66:67], 0, s[92:93]
	v_lshl_add_u64 v[66:67], v[66:67], 0, s[36:37]
	v_lshlrev_b64 v[68:69], 8, v[68:69]
	v_lshlrev_b64 v[66:67], 8, v[66:67]
	v_lshl_add_u64 v[68:69], v[174:175], 0, v[68:69]
	v_lshl_add_u64 v[74:75], v[174:175], 0, v[66:67]
	global_load_dwordx4 v[94:97], v[68:69], off
	global_load_dwordx4 v[82:85], v[68:69], off offset:64
	global_load_dwordx4 v[86:89], v[68:69], off offset:128
	global_load_dwordx4 v[90:93], v[68:69], off offset:192
	global_load_dwordx4 v[78:81], v[74:75], off
	s_nop 0
	global_load_dwordx4 v[66:69], v[74:75], off offset:64
	global_load_dwordx4 v[70:73], v[74:75], off offset:128
	s_nop 0
	global_load_dwordx4 v[74:77], v[74:75], off offset:192
	s_and_saveexec_b64 s[54:55], s[2:3]
	s_lshl_b64 vcc, s[56:57], 7
	v_lshl_add_u64 v[98:99], vcc, 0, v[170:171]
	v_lshlrev_b64 v[98:99], 2, v[98:99]
	v_lshl_add_u64 v[100:101], s[26:27], 0, v[98:99]
	global_load_dword v0, v[100:101], off
	v_lshl_add_u64 v[100:101], s[28:29], 0, v[98:99]
	global_load_dword v100, v[100:101], off
	v_lshl_add_u64 v[98:99], s[74:75], 0, v[98:99]
	global_load_dword v98, v[98:99], off
	s_or_b64 exec, exec, s[54:55]
	s_waitcnt vmcnt(0)
	s_barrier
	s_and_saveexec_b64 s[54:55], s[2:3]
	s_cbranch_execz .LBB0_594
	ds_write2st64_b32 v163, v0, v100 offset1:2
	v_sub_f32_e32 v0, v100, v0
	ds_write2st64_b32 v163, v98, v0 offset0:4 offset1:8
